# rwkv_pre S3: static priority raise for the two solver waves for the duration of the stage
# baseline (speedup 1.0000x reference)
.LBB0_622:
	v_mov_b32_e32 v18, v187
	s_waitcnt lgkmcnt(0)
	s_barrier
	v_readlane_b32 s2, v252, 43
	v_bfe_u32 v32, v18, 4, 2
	v_ashrrev_i32_e32 v0, 3, v18
	v_and_b32_e32 v19, 15, v18
	v_and_b32_e32 v33, -16, v0
	v_bfi_b32 v20, -16, v0, v18
	v_lshl_add_u32 v0, v32, 4, 0
	v_lshrrev_b32_e32 v18, 1, v18
	v_mad_u64_u32 v[30:31], s[0:1], v20, s40, v[0:1]
	v_and_b32_e32 v166, 32, v18
	v_readlane_b32 s0, v252, 41
	v_or_b32_e32 v167, v166, v19
	v_mad_u32_u24 v26, v167, s40, v0
	v_lshl_add_u32 v31, v19, 2, s0
	ds_read_b128 v[18:21], v30 offset:64512
	ds_read_b128 v[22:25], v26 offset:55296
	ds_read_b128 v[2:5], v30 offset:64576
	ds_read_b128 v[6:9], v26 offset:55360
	v_or_b32_e32 v10, 16, v167
	v_mad_u32_u24 v0, v10, s40, v0
	ds_read_b128 v[10:13], v0 offset:55296
	ds_read_b128 v[14:17], v0 offset:55360
	v_readlane_b32 s4, v252, 42
	s_mov_b32 s11, 0
	v_lshlrev_b32_e32 v175, 8, v33
	v_lshlrev_b32_e32 v174, 2, v166
	v_lshl_or_b32 v175, v32, 10, v175
	v_add3_u32 v31, v31, v174, v175
	s_waitcnt lgkmcnt(4)
	v_mfma_f32_16x16x32_bf16 v[176:179], v[18:21], v[22:25], 0
	s_waitcnt lgkmcnt(2)
	v_mfma_f32_16x16x32_bf16 v[176:179], v[2:5], v[6:9], v[176:179]
	s_waitcnt lgkmcnt(1)
	v_mfma_f32_16x16x32_bf16 v[240:243], v[18:21], v[10:13], 0
	s_waitcnt lgkmcnt(0)
	v_mfma_f32_16x16x32_bf16 v[240:243], v[2:5], v[14:17], v[240:243]
	s_nop 3
	ds_write_b32 v31, v176
	ds_write_b32 v31, v177 offset:256
	ds_write_b32 v31, v178 offset:512
	ds_write_b32 v31, v179 offset:768
	ds_write_b32 v31, v240 offset:64
	ds_write_b32 v31, v241 offset:320
	ds_write_b32 v31, v242 offset:576
	ds_write_b32 v31, v243 offset:832
	v_mov_b32_e32 v18, v187
	s_waitcnt lgkmcnt(0)
	s_barrier
	v_mov_b32_e32 v22, s2
	v_ashrrev_i32_e32 v20, 6, v18
	v_and_b32_e32 v21, 15, v18
	v_cmp_gt_i32_e64 s[0:1], 2, v20
	v_cmp_gt_i32_e32 vcc, 4, v20
	v_lshlrev_b32_e32 v20, 4, v20
	v_mov_b32_e32 v23, s96
	v_and_or_b32 v20, v20, 48, v21
	v_cndmask_b32_e32 v24, v22, v23, vcc
	v_mul_u32_u24_e32 v20, 0x90, v20
	v_and_b32_e32 v25, 48, v18
	v_and_b32_e32 v19, 63, v18
	v_add3_u32 v166, v24, v20, v25
	v_lshlrev_b32_e32 v20, 7, v18
	v_and_b32_e32 v24, 0xffffffc0, v18
	v_cmp_lt_u32_e64 s[2:3], 63, v18
	v_cmp_gt_u32_e32 vcc, 64, v18
	v_and_b32_e32 v18, 0x3fffffc0, v18
	v_lshlrev_b32_e32 v0, 2, v19
	v_and_b32_e32 v20, 0x1800, v20
	v_lshlrev_b32_e32 v18, 2, v18
	v_add_u32_e32 v20, s4, v20
	v_lshlrev_b32_e32 v26, 2, v21
	v_add3_u32 v168, s4, v0, v18
	v_cndmask_b32_e32 v18, v22, v23, vcc
	v_add3_u32 v167, v20, v24, v26
	v_mad_u32_u24 v169, v19, s40, v18
	v_mad_u32_u24 v170, v21, s40, v25
	v_lshlrev_b32_e32 v171, 1, v19
	v_readfirstlane_b32 s14, v187
	s_cmp_lt_u32 s14, 0x80
	s_cbranch_scc0 .Ls3_noprio
	s_setprio 2
.Ls3_noprio:
	s_branch .LBB0_625

.LBB0_638:
	s_setprio 0
	v_mov_b32_e32 v0, v187
	s_ashr_i32 s11, s10, 31
	s_barrier
	s_waitcnt vmcnt(0)
	s_lshl_b64 s[0:1], s[10:11], 13
	v_lshrrev_b32_e32 v18, 6, v0
	v_and_b32_e32 v166, 15, v0
	v_and_b32_e32 v167, 48, v0
	v_readfirstlane_b32 s2, v18
	v_and_b32_e32 v168, 63, v0
	v_mul_u32_u24_e32 v169, 0x90, v166
	s_and_b32 s3, s2, 1
	s_lshr_b32 s4, s2, 1
	v_add_u32_e32 v169, v169, v167
	s_mul_i32 s5, s3, 0x1200
	s_lshl_b32 s12, s3, 12
	s_cmp_lt_u32 s4, 2
	s_cbranch_scc1 .Ls4_qh
	s_cmp_eq_u32 s4, 2
	s_cbranch_scc1 .Ls4_a
	s_add_u32 s14, s36, s0
	s_addc_u32 s15, s37, s1
	v_add_u32_e32 v170, s5, v169
	v_add_u32_e32 v171, 0x18c00, v169
	s_lshl_b32 s13, s3, 7
	v_add_u32_e32 v172, 0x27c00, v167
	v_add_u32_e32 v172, s13, v172
	v_lshl_add_u32 v173, v168, 3, s12
	ds_read_b128 v[2:5], v170 offset:36864
	ds_read_b128 v[6:9], v171 offset:0
	ds_read_b128 v[10:13], v170 offset:36928
	ds_read_b128 v[14:17], v171 offset:64
	ds_read_b128 v[174:177], v170 offset:46080
	ds_read_b128 v[178:181], v169 offset:55296
	ds_read_b128 v[240:243], v170 offset:46144
	ds_read_b128 v[244:247], v169 offset:55360
	ds_read_b128 v[218:221], v172 offset:0
	s_waitcnt lgkmcnt(7)
	v_mfma_f32_16x16x32_bf16 v[24:27], v[2:5], v[6:9], 0
	ds_read_b128 v[2:5], v170 offset:36864
	ds_read_b128 v[6:9], v171 offset:2304
	s_waitcnt lgkmcnt(7)
	v_mfma_f32_16x16x32_bf16 v[24:27], v[10:13], v[14:17], v[24:27]
	ds_read_b128 v[10:13], v170 offset:36928
	ds_read_b128 v[14:17], v171 offset:2368
	s_waitcnt lgkmcnt(7)
	v_mfma_f32_16x16x32_bf16 v[24:27], v[174:177], v[178:181], v[24:27]
	ds_read_b128 v[174:177], v170 offset:46080
	ds_read_b128 v[178:181], v169 offset:57600
	s_waitcnt lgkmcnt(7)
	v_mfma_f32_16x16x32_bf16 v[24:27], v[240:243], v[244:247], v[24:27]
	ds_read_b128 v[240:243], v170 offset:46144
	ds_read_b128 v[244:247], v169 offset:57664
	ds_read_b128 v[18:21], v172 offset:0
	s_waitcnt lgkmcnt(9)
	s_nop 3
	v_pk_mul_f32 v[24:25], v[24:25], v[218:219]
	v_pk_mul_f32 v[26:27], v[26:27], v[220:221]
	v_cvt_pk_bf16_f32 v32, v24, v25
	v_cvt_pk_bf16_f32 v33, v26, v27
	global_store_dwordx2 v173, v[32:33], s[14:15] offset:0
	s_waitcnt lgkmcnt(7)
	v_mfma_f32_16x16x32_bf16 v[28:31], v[2:5], v[6:9], 0
	ds_read_b128 v[2:5], v170 offset:36864
	ds_read_b128 v[6:9], v171 offset:4608
	s_waitcnt lgkmcnt(7)
	v_mfma_f32_16x16x32_bf16 v[28:31], v[10:13], v[14:17], v[28:31]
	ds_read_b128 v[10:13], v170 offset:36928
	ds_read_b128 v[14:17], v171 offset:4672
	s_waitcnt lgkmcnt(7)
	v_mfma_f32_16x16x32_bf16 v[28:31], v[174:177], v[178:181], v[28:31]
	ds_read_b128 v[174:177], v170 offset:46080
	ds_read_b128 v[178:181], v169 offset:59904
	s_waitcnt lgkmcnt(7)
	v_mfma_f32_16x16x32_bf16 v[28:31], v[240:243], v[244:247], v[28:31]
	ds_read_b128 v[240:243], v170 offset:46144
	ds_read_b128 v[244:247], v169 offset:59968
	ds_read_b128 v[218:221], v172 offset:0
	s_waitcnt lgkmcnt(9)
	s_nop 3
	v_pk_mul_f32 v[28:29], v[28:29], v[18:19]
	v_pk_mul_f32 v[30:31], v[30:31], v[20:21]
	v_cvt_pk_bf16_f32 v22, v28, v29
	v_cvt_pk_bf16_f32 v23, v30, v31
	global_store_dwordx2 v173, v[22:23], s[14:15] offset:512
	s_waitcnt lgkmcnt(7)
	v_mfma_f32_16x16x32_bf16 v[24:27], v[2:5], v[6:9], 0
	ds_read_b128 v[2:5], v170 offset:36864
	ds_read_b128 v[6:9], v171 offset:6912
	s_waitcnt lgkmcnt(7)
	v_mfma_f32_16x16x32_bf16 v[24:27], v[10:13], v[14:17], v[24:27]
	ds_read_b128 v[10:13], v170 offset:36928
	ds_read_b128 v[14:17], v171 offset:6976
	s_waitcnt lgkmcnt(7)
	v_mfma_f32_16x16x32_bf16 v[24:27], v[174:177], v[178:181], v[24:27]
	ds_read_b128 v[174:177], v170 offset:46080
	ds_read_b128 v[178:181], v169 offset:62208
	s_waitcnt lgkmcnt(7)
	v_mfma_f32_16x16x32_bf16 v[24:27], v[240:243], v[244:247], v[24:27]
	ds_read_b128 v[240:243], v170 offset:46144
	ds_read_b128 v[244:247], v169 offset:62272
	ds_read_b128 v[18:21], v172 offset:0
	s_waitcnt lgkmcnt(9)
	s_nop 3
	v_pk_mul_f32 v[24:25], v[24:25], v[218:219]
	v_pk_mul_f32 v[26:27], v[26:27], v[220:221]
	v_cvt_pk_bf16_f32 v32, v24, v25
	v_cvt_pk_bf16_f32 v33, v26, v27
	global_store_dwordx2 v173, v[32:33], s[14:15] offset:1024
	s_waitcnt lgkmcnt(7)
	v_mfma_f32_16x16x32_bf16 v[28:31], v[2:5], v[6:9], 0
	ds_read_b128 v[2:5], v170 offset:39168
	ds_read_b128 v[6:9], v171 offset:0
	s_waitcnt lgkmcnt(7)
	v_mfma_f32_16x16x32_bf16 v[28:31], v[10:13], v[14:17], v[28:31]
	ds_read_b128 v[10:13], v170 offset:39232
	ds_read_b128 v[14:17], v171 offset:64
	s_waitcnt lgkmcnt(7)
	v_mfma_f32_16x16x32_bf16 v[28:31], v[174:177], v[178:181], v[28:31]
	ds_read_b128 v[174:177], v170 offset:48384
	ds_read_b128 v[178:181], v169 offset:55296
	s_waitcnt lgkmcnt(7)
	v_mfma_f32_16x16x32_bf16 v[28:31], v[240:243], v[244:247], v[28:31]
	ds_read_b128 v[240:243], v170 offset:48448
	ds_read_b128 v[244:247], v169 offset:55360
	ds_read_b128 v[218:221], v172 offset:64
	s_waitcnt lgkmcnt(9)
	s_nop 3
	v_pk_mul_f32 v[28:29], v[28:29], v[18:19]
	v_pk_mul_f32 v[30:31], v[30:31], v[20:21]
	v_cvt_pk_bf16_f32 v22, v28, v29
	v_cvt_pk_bf16_f32 v23, v30, v31
	global_store_dwordx2 v173, v[22:23], s[14:15] offset:1536
	s_waitcnt lgkmcnt(7)
	v_mfma_f32_16x16x32_bf16 v[24:27], v[2:5], v[6:9], 0
	ds_read_b128 v[2:5], v170 offset:39168
	ds_read_b128 v[6:9], v171 offset:2304
	s_waitcnt lgkmcnt(7)
	v_mfma_f32_16x16x32_bf16 v[24:27], v[10:13], v[14:17], v[24:27]
	ds_read_b128 v[10:13], v170 offset:39232
	ds_read_b128 v[14:17], v171 offset:2368
	s_waitcnt lgkmcnt(7)
	v_mfma_f32_16x16x32_bf16 v[24:27], v[174:177], v[178:181], v[24:27]
	ds_read_b128 v[174:177], v170 offset:48384
	ds_read_b128 v[178:181], v169 offset:57600
	s_waitcnt lgkmcnt(7)
	v_mfma_f32_16x16x32_bf16 v[24:27], v[240:243], v[244:247], v[24:27]
	ds_read_b128 v[240:243], v170 offset:48448
	ds_read_b128 v[244:247], v169 offset:57664
	ds_read_b128 v[18:21], v172 offset:64
	s_waitcnt lgkmcnt(9)
	s_nop 3
	v_pk_mul_f32 v[24:25], v[24:25], v[218:219]
	v_pk_mul_f32 v[26:27], v[26:27], v[220:221]
	v_cvt_pk_bf16_f32 v32, v24, v25
	v_cvt_pk_bf16_f32 v33, v26, v27
	global_store_dwordx2 v173, v[32:33], s[14:15] offset:2048
	s_waitcnt lgkmcnt(7)
	v_mfma_f32_16x16x32_bf16 v[28:31], v[2:5], v[6:9], 0
	ds_read_b128 v[2:5], v170 offset:39168
	ds_read_b128 v[6:9], v171 offset:4608
	s_waitcnt lgkmcnt(7)
	v_mfma_f32_16x16x32_bf16 v[28:31], v[10:13], v[14:17], v[28:31]
	ds_read_b128 v[10:13], v170 offset:39232
	ds_read_b128 v[14:17], v171 offset:4672
	s_waitcnt lgkmcnt(7)
	v_mfma_f32_16x16x32_bf16 v[28:31], v[174:177], v[178:181], v[28:31]
	ds_read_b128 v[174:177], v170 offset:48384
	ds_read_b128 v[178:181], v169 offset:59904
	s_waitcnt lgkmcnt(7)
	v_mfma_f32_16x16x32_bf16 v[28:31], v[240:243], v[244:247], v[28:31]
	ds_read_b128 v[240:243], v170 offset:48448
	ds_read_b128 v[244:247], v169 offset:59968
	ds_read_b128 v[218:221], v172 offset:64
	s_waitcnt lgkmcnt(9)
	s_nop 3
	v_pk_mul_f32 v[28:29], v[28:29], v[18:19]
	v_pk_mul_f32 v[30:31], v[30:31], v[20:21]
	v_cvt_pk_bf16_f32 v22, v28, v29
	v_cvt_pk_bf16_f32 v23, v30, v31
	global_store_dwordx2 v173, v[22:23], s[14:15] offset:2560
	s_waitcnt lgkmcnt(7)
	v_mfma_f32_16x16x32_bf16 v[24:27], v[2:5], v[6:9], 0
	ds_read_b128 v[2:5], v170 offset:39168
	ds_read_b128 v[6:9], v171 offset:6912
	s_waitcnt lgkmcnt(7)
	v_mfma_f32_16x16x32_bf16 v[24:27], v[10:13], v[14:17], v[24:27]
	ds_read_b128 v[10:13], v170 offset:39232
	ds_read_b128 v[14:17], v171 offset:6976
	s_waitcnt lgkmcnt(7)
	v_mfma_f32_16x16x32_bf16 v[24:27], v[174:177], v[178:181], v[24:27]
	ds_read_b128 v[174:177], v170 offset:48384
	ds_read_b128 v[178:181], v169 offset:62208
	s_waitcnt lgkmcnt(7)
	v_mfma_f32_16x16x32_bf16 v[24:27], v[240:243], v[244:247], v[24:27]
	ds_read_b128 v[240:243], v170 offset:48448
	ds_read_b128 v[244:247], v169 offset:62272
	ds_read_b128 v[18:21], v172 offset:64
	s_waitcnt lgkmcnt(9)
	s_nop 3
	v_pk_mul_f32 v[24:25], v[24:25], v[218:219]
	v_pk_mul_f32 v[26:27], v[26:27], v[220:221]
	v_cvt_pk_bf16_f32 v32, v24, v25
	v_cvt_pk_bf16_f32 v33, v26, v27
	global_store_dwordx2 v173, v[32:33], s[14:15] offset:3072
	s_waitcnt lgkmcnt(7)
	v_mfma_f32_16x16x32_bf16 v[28:31], v[2:5], v[6:9], 0
	s_waitcnt lgkmcnt(5)
	v_mfma_f32_16x16x32_bf16 v[28:31], v[10:13], v[14:17], v[28:31]
	s_waitcnt lgkmcnt(3)
	v_mfma_f32_16x16x32_bf16 v[28:31], v[174:177], v[178:181], v[28:31]
	s_waitcnt lgkmcnt(1)
	v_mfma_f32_16x16x32_bf16 v[28:31], v[240:243], v[244:247], v[28:31]
	s_waitcnt lgkmcnt(0)
	s_nop 6
	v_pk_mul_f32 v[28:29], v[28:29], v[18:19]
	v_pk_mul_f32 v[30:31], v[30:31], v[20:21]
	v_cvt_pk_bf16_f32 v22, v28, v29
	v_cvt_pk_bf16_f32 v23, v30, v31
	global_store_dwordx2 v173, v[22:23], s[14:15] offset:3584
	s_branch .LBB0_600
